# LayerNorm-1 panel exchange: four partner slots loaded together; redundant L1 invalidate before the sc1 slot loads dropped
# speedup vs baseline: 1.0082x; 1.0027x over previous
.LBB0_1275:
	s_waitcnt vmcnt(0)
	s_and_b64 exec, exec, s[4:5]
	s_cbranch_execz .LBB0_1277
	v_readlane_b32 s4, v253, 56
	v_cndmask_b32_e64 v3, 0, 1, s[38:39]
	s_nop 0
	v_mov_b32_e32 v4, s4
	ds_write_b32 v4, v3

.LBB0_1278:
	v_readlane_b32 s4, v253, 56
	s_waitcnt vmcnt(0) lgkmcnt(0)
	s_barrier
	s_nop 0
	v_mov_b32_e32 v3, s4
	ds_read_b32 v3, v3
	s_and_saveexec_b64 s[4:5], s[2:3]
	s_cbranch_execz .LBB0_1280
	v_lshlrev_b64 v[0:1], 5, v[0:1]
	v_lshl_add_u64 v[0:1], s[20:21], 0, v[0:1]
	global_load_dwordx2 v[4:5], v[0:1], off sc1
	global_load_dwordx2 v[6:7], v[0:1], off offset:8 sc1
	global_load_dwordx2 v[8:9], v[0:1], off offset:16 sc1
	global_load_dwordx2 v[10:11], v[0:1], off offset:24 sc1
	v_lshl_add_u32 v2, v2, 3, 0
	v_add_u32_e32 v2, 0x21000, v2
	s_waitcnt vmcnt(3)
	v_add_f32_e32 v12, 0, v4
	s_waitcnt vmcnt(2)
	v_add_f32_e32 v12, v12, v6
	s_waitcnt vmcnt(1)
	v_add_f32_e32 v12, v12, v8
	s_waitcnt vmcnt(0)
	v_add_f32_e32 v1, v12, v10
	v_fmamk_f32 v4, v1, 0xbe800000, v4
	v_mul_f32_e32 v12, 0x43800000, v4
	v_fmac_f32_e32 v5, v4, v12
	v_add_f32_e32 v4, 0, v5
	v_fmamk_f32 v5, v1, 0xbe800000, v6
	v_mul_f32_e32 v6, 0x43800000, v5
	v_fmac_f32_e32 v7, v5, v6
	v_fmamk_f32 v5, v1, 0xbe800000, v8
	v_mul_f32_e32 v0, 0x3e800000, v1
	v_mul_f32_e32 v6, 0x43800000, v5
	v_fmamk_f32 v1, v1, 0xbe800000, v10
	v_add_f32_e32 v4, v7, v4
	v_fmac_f32_e32 v9, v5, v6
	v_mul_f32_e32 v5, 0x43800000, v1
	v_add_f32_e32 v4, v9, v4
	v_fmac_f32_e32 v11, v1, v5
	v_add_f32_e32 v1, v11, v4
	v_fmamk_f32 v1, v1, 0x3a800000, v224
	v_cmp_gt_f32_e32 vcc, s1, v1
	v_mul_f32_e32 v4, 0x4f800000, v1
	s_nop 0
	v_cndmask_b32_e32 v1, v1, v4, vcc
	v_sqrt_f32_e32 v4, v1
	s_nop 0
	v_add_u32_e32 v5, -1, v4
	v_fma_f32 v6, -v5, v4, v1
	v_cmp_ge_f32_e64 s[2:3], 0, v6
	v_add_u32_e32 v6, 1, v4
	s_nop 0
	v_cndmask_b32_e64 v5, v4, v5, s[2:3]
	v_fma_f32 v4, -v6, v4, v1
	v_cmp_lt_f32_e64 s[2:3], 0, v4
	s_nop 1
	v_cndmask_b32_e64 v4, v5, v6, s[2:3]
	v_mul_f32_e32 v5, 0x37800000, v4
	v_cndmask_b32_e32 v4, v4, v5, vcc
	v_cmp_class_f32_e32 vcc, v1, v240
	s_nop 1
	v_cndmask_b32_e32 v1, v4, v1, vcc
	v_div_scale_f32 v4, s[2:3], v1, v1, 1.0
	v_rcp_f32_e32 v5, v4
	s_nop 0
	v_fma_f32 v6, -v4, v5, 1.0
	v_fmac_f32_e32 v5, v6, v5
	v_div_scale_f32 v6, vcc, 1.0, v1, 1.0
	v_mul_f32_e32 v7, v6, v5
	v_fma_f32 v8, -v4, v7, v6
	v_fmac_f32_e32 v7, v8, v5
	v_fma_f32 v4, -v4, v7, v6
	v_div_fmas_f32 v4, v4, v5, v7
	v_div_fixup_f32 v1, v4, v1, 1.0
	ds_write_b64 v2, v[0:1]
